# on top of v43: grid barrier non-leader workgroups poll the global generation word directly instead of their XCD leader's relayed generation (one hop less on the release path)
# speedup vs baseline: 1.0015x; 1.0003x over previous
; __device__ __forceinline__ unsigned xb_ld(unsigned* p)              { return __hip_atomic_load(p, __ATOMIC_RELAXED, __HIP_MEMORY_SCOPE_AGENT); }
; __device__ __forceinline__ unsigned xb_add(unsigned* p, unsigned v) { return __hip_atomic_fetch_add(p, v, __ATOMIC_RELAXED, __HIP_MEMORY_SCOPE_AGENT); }
; #define XB_SPIN(cond, bar) do { unsigned _sp = 0; while (cond) { __builtin_amdgcn_s_sleep(1); \
;     if ((++_sp & 255u) == 0u) { if (xb_ld(&(bar)[XB_TMO])) break; if (_sp > XB_SPIN_CAP) { atomicAdd(&(bar)[XB_TMO], 1u); break; } } } } while (0)
; __device__ __forceinline__ void xcd_barrier(const XcdBarrier& b) {
;     ...
;         const unsigned old = xb_add(&bar[XB_XSUB(b.x)], 1u);
;         const unsigned gen = old / nloc;
;         if (old + 1u == (gen + 1u) * nloc) {
;             __builtin_amdgcn_fence(__ATOMIC_RELEASE, "agent");
;             asm volatile("s_waitcnt vmcnt(0)" ::: "memory");
;             const unsigned og = xb_add(&bar[XB_TOP], 1u);
;             const unsigned tg = og / nx;
;             if (og + 1u == (tg + 1u) * nx) xb_add(&bar[XB_TOPGEN], 1u);
;             else XB_SPIN(xb_ld(&bar[XB_TOPGEN]) == tg, bar);
;             __builtin_amdgcn_fence(__ATOMIC_ACQUIRE, "agent");
;             xb_add(&bar[XB_XGEN(b.x)], 1u);
;             asm volatile("s_waitcnt vmcnt(0)" ::: "memory");
;         } else {
;             XB_SPIN(xb_ld(&bar[XB_XGEN(b.x)]) == gen, bar);
;             __builtin_amdgcn_fence(__ATOMIC_ACQUIRE, "agent");
;             asm volatile("s_waitcnt vmcnt(0)" ::: "memory");
;         }
.LBB0_148:
	v_readlane_b32 s3, v254, 29
	s_lshl_b32 s3, s3, 8
	v_readlane_b32 s6, v254, 27
	v_readlane_b32 s7, v254, 28
	s_add_u32 s6, s6, s3
	s_addc_u32 s7, s7, 0
	v_mov_b32_e32 v2, 0x1000
	v_mov_b32_e32 v4, 1
	v_sub_u32_e32 v5, 0, v3
	global_atomic_add v4, v2, v4, s[6:7] offset:1024 sc0
	v_cvt_f32_u32_e32 v2, v3
	v_rcp_iflag_f32_e32 v2, v2
	s_nop 0
	v_mul_f32_e32 v2, 0x4f7ffffe, v2
	v_cvt_u32_f32_e32 v2, v2
	v_mul_lo_u32 v5, v5, v2
	v_mul_hi_u32 v5, v2, v5
	v_add_u32_e32 v2, v2, v5
	s_waitcnt vmcnt(0)
	v_mul_hi_u32 v2, v4, v2
	v_mul_lo_u32 v5, v2, v3
	v_sub_u32_e32 v5, v4, v5
	v_add_u32_e32 v6, 1, v2
	v_cmp_ge_u32_e32 vcc, v5, v3
	v_add_u32_e32 v4, 1, v4
	s_nop 0
	v_cndmask_b32_e32 v2, v2, v6, vcc
	v_sub_u32_e32 v6, v5, v3
	v_cndmask_b32_e32 v5, v5, v6, vcc
	v_add_u32_e32 v6, 1, v2
	v_cmp_ge_u32_e32 vcc, v5, v3
	s_nop 1
	v_cndmask_b32_e32 v2, v2, v6, vcc
	v_mul_lo_u32 v5, v3, v2
	v_add_u32_e32 v3, v5, v3
	v_cmp_ne_u32_e32 vcc, v4, v3
	s_and_saveexec_b64 s[8:9], vcc
	s_xor_b64 s[8:9], exec, s[8:9]
	s_cbranch_execz .LBB0_162
	s_waitcnt lgkmcnt(0)
	v_mov_b32_e32 v1, 0x2000
	s_add_u32 s36, s30, 0x7500
	s_addc_u32 s37, s31, 0
	v_mov_b32_e32 v1, 0
	global_load_dword v1, v1, s[36:37] sc1
	s_waitcnt vmcnt(0)
	v_cmp_eq_u32_e32 vcc, v1, v2
	s_and_saveexec_b64 s[10:11], vcc
	s_cbranch_execz .LBB0_161
	s_add_u32 s14, s30, 0x4200
	s_addc_u32 s15, s31, 0
	s_mov_b32 s3, 1
	s_mov_b64 s[38:39], 0
	v_mov_b32_e32 v1, 0
	s_branch .LBB0_152

; __device__ __forceinline__ unsigned xb_ld(unsigned* p)              { return __hip_atomic_load(p, __ATOMIC_RELAXED, __HIP_MEMORY_SCOPE_AGENT); }
; __device__ __forceinline__ unsigned xb_add(unsigned* p, unsigned v) { return __hip_atomic_fetch_add(p, v, __ATOMIC_RELAXED, __HIP_MEMORY_SCOPE_AGENT); }
; #define XB_SPIN(cond, bar) do { unsigned _sp = 0; while (cond) { __builtin_amdgcn_s_sleep(1); \
;     if ((++_sp & 255u) == 0u) { if (xb_ld(&(bar)[XB_TMO])) break; if (_sp > XB_SPIN_CAP) { atomicAdd(&(bar)[XB_TMO], 1u); break; } } } } while (0)
; __device__ __forceinline__ void xcd_barrier(const XcdBarrier& b) {
;     ...
;         const unsigned old = xb_add(&bar[XB_XSUB(b.x)], 1u);
;         const unsigned gen = old / nloc;
;         if (old + 1u == (gen + 1u) * nloc) {
;             __builtin_amdgcn_fence(__ATOMIC_RELEASE, "agent");
;             asm volatile("s_waitcnt vmcnt(0)" ::: "memory");
;             const unsigned og = xb_add(&bar[XB_TOP], 1u);
;             const unsigned tg = og / nx;
;             if (og + 1u == (tg + 1u) * nx) xb_add(&bar[XB_TOPGEN], 1u);
;             else XB_SPIN(xb_ld(&bar[XB_TOPGEN]) == tg, bar);
;             __builtin_amdgcn_fence(__ATOMIC_ACQUIRE, "agent");
;             xb_add(&bar[XB_XGEN(b.x)], 1u);
;             asm volatile("s_waitcnt vmcnt(0)" ::: "memory");
;         } else {
;             XB_SPIN(xb_ld(&bar[XB_XGEN(b.x)]) == gen, bar);
;             __builtin_amdgcn_fence(__ATOMIC_ACQUIRE, "agent");
;             asm volatile("s_waitcnt vmcnt(0)" ::: "memory");
;         }
.LBB0_970:
	v_readlane_b32 s3, v254, 29
	s_lshl_b32 s3, s3, 8
	v_readlane_b32 s4, v254, 27
	v_readlane_b32 s5, v254, 28
	s_add_u32 s4, s4, s3
	s_addc_u32 s5, s5, 0
	v_mov_b32_e32 v2, 0x1000
	v_mov_b32_e32 v4, 1
	v_sub_u32_e32 v5, 0, v3
	global_atomic_add v4, v2, v4, s[4:5] offset:1024 sc0
	v_cvt_f32_u32_e32 v2, v3
	v_rcp_iflag_f32_e32 v2, v2
	s_nop 0
	v_mul_f32_e32 v2, 0x4f7ffffe, v2
	v_cvt_u32_f32_e32 v2, v2
	v_mul_lo_u32 v5, v5, v2
	v_mul_hi_u32 v5, v2, v5
	v_add_u32_e32 v2, v2, v5
	s_waitcnt vmcnt(0)
	v_mul_hi_u32 v2, v4, v2
	v_mul_lo_u32 v5, v2, v3
	v_sub_u32_e32 v5, v4, v5
	v_add_u32_e32 v6, 1, v2
	v_cmp_ge_u32_e32 vcc, v5, v3
	v_add_u32_e32 v4, 1, v4
	s_nop 0
	v_cndmask_b32_e32 v2, v2, v6, vcc
	v_sub_u32_e32 v6, v5, v3
	v_cndmask_b32_e32 v5, v5, v6, vcc
	v_add_u32_e32 v6, 1, v2
	v_cmp_ge_u32_e32 vcc, v5, v3
	s_nop 1
	v_cndmask_b32_e32 v2, v2, v6, vcc
	v_mul_lo_u32 v5, v3, v2
	v_add_u32_e32 v3, v5, v3
	v_cmp_ne_u32_e32 vcc, v4, v3
	s_and_saveexec_b64 s[6:7], vcc
	s_xor_b64 s[6:7], exec, s[6:7]
	s_cbranch_execz .LBB0_984
	s_waitcnt lgkmcnt(0)
	v_mov_b32_e32 v1, 0x2000
	s_add_u32 s12, s30, 0x7500
	s_addc_u32 s13, s31, 0
	v_mov_b32_e32 v1, 0
	global_load_dword v1, v1, s[12:13] sc1
	s_waitcnt vmcnt(0)
	v_cmp_eq_u32_e32 vcc, v1, v2
	s_and_saveexec_b64 s[8:9], vcc
	s_cbranch_execz .LBB0_983
	s_add_u32 s10, s30, 0x4200
	s_addc_u32 s11, s31, 0
	s_mov_b32 s3, 1
	s_mov_b64 s[14:15], 0
	v_mov_b32_e32 v1, 0
	s_branch .LBB0_974

; __device__ __forceinline__ unsigned xb_ld(unsigned* p)              { return __hip_atomic_load(p, __ATOMIC_RELAXED, __HIP_MEMORY_SCOPE_AGENT); }
; __device__ __forceinline__ unsigned xb_add(unsigned* p, unsigned v) { return __hip_atomic_fetch_add(p, v, __ATOMIC_RELAXED, __HIP_MEMORY_SCOPE_AGENT); }
; #define XB_SPIN(cond, bar) do { unsigned _sp = 0; while (cond) { __builtin_amdgcn_s_sleep(1); \
;     if ((++_sp & 255u) == 0u) { if (xb_ld(&(bar)[XB_TMO])) break; if (_sp > XB_SPIN_CAP) { atomicAdd(&(bar)[XB_TMO], 1u); break; } } } } while (0)
; __device__ __forceinline__ void xcd_barrier(const XcdBarrier& b) {
;     ...
;         const unsigned old = xb_add(&bar[XB_XSUB(b.x)], 1u);
;         const unsigned gen = old / nloc;
;         if (old + 1u == (gen + 1u) * nloc) {
;             __builtin_amdgcn_fence(__ATOMIC_RELEASE, "agent");
;             asm volatile("s_waitcnt vmcnt(0)" ::: "memory");
;             const unsigned og = xb_add(&bar[XB_TOP], 1u);
;             const unsigned tg = og / nx;
;             if (og + 1u == (tg + 1u) * nx) xb_add(&bar[XB_TOPGEN], 1u);
;             else XB_SPIN(xb_ld(&bar[XB_TOPGEN]) == tg, bar);
;             __builtin_amdgcn_fence(__ATOMIC_ACQUIRE, "agent");
;             xb_add(&bar[XB_XGEN(b.x)], 1u);
;             asm volatile("s_waitcnt vmcnt(0)" ::: "memory");
;         } else {
;             XB_SPIN(xb_ld(&bar[XB_XGEN(b.x)]) == gen, bar);
;             __builtin_amdgcn_fence(__ATOMIC_ACQUIRE, "agent");
;             asm volatile("s_waitcnt vmcnt(0)" ::: "memory");
;         }
.LBB0_1065:
	v_readlane_b32 s4, v254, 29
	s_lshl_b32 s4, s4, 8
	v_readlane_b32 s6, v254, 27
	v_readlane_b32 s7, v254, 28
	s_add_u32 s4, s6, s4
	s_addc_u32 s5, s7, 0
	v_mov_b32_e32 v2, 0x1000
	v_mov_b32_e32 v4, 1
	global_atomic_add v4, v2, v4, s[4:5] offset:1024 sc0
	v_cvt_f32_u32_e32 v2, v3
	v_sub_u32_e32 v5, 0, v3
	v_rcp_iflag_f32_e32 v2, v2
	s_nop 0
	v_mul_f32_e32 v2, 0x4f7ffffe, v2
	v_cvt_u32_f32_e32 v2, v2
	v_mul_lo_u32 v5, v5, v2
	v_mul_hi_u32 v5, v2, v5
	v_add_u32_e32 v2, v2, v5
	s_waitcnt vmcnt(0)
	v_mul_hi_u32 v2, v4, v2
	v_mul_lo_u32 v5, v2, v3
	v_sub_u32_e32 v5, v4, v5
	v_add_u32_e32 v6, 1, v2
	v_cmp_ge_u32_e32 vcc, v5, v3
	v_add_u32_e32 v4, 1, v4
	s_nop 0
	v_cndmask_b32_e32 v2, v2, v6, vcc
	v_sub_u32_e32 v6, v5, v3
	v_cndmask_b32_e32 v5, v5, v6, vcc
	v_add_u32_e32 v6, 1, v2
	v_cmp_ge_u32_e32 vcc, v5, v3
	s_nop 1
	v_cndmask_b32_e32 v2, v2, v6, vcc
	v_mul_lo_u32 v5, v3, v2
	v_add_u32_e32 v3, v5, v3
	v_cmp_ne_u32_e32 vcc, v4, v3
	s_and_saveexec_b64 s[6:7], vcc
	s_xor_b64 s[6:7], exec, s[6:7]
	s_cbranch_execz .LBB0_1079
	s_waitcnt lgkmcnt(0)
	v_mov_b32_e32 v1, 0x2000
	s_add_u32 s12, s30, 0x7500
	s_addc_u32 s13, s31, 0
	v_mov_b32_e32 v1, 0
	global_load_dword v1, v1, s[12:13] sc1
	s_waitcnt vmcnt(0)
	v_cmp_eq_u32_e32 vcc, v1, v2
	s_and_saveexec_b64 s[8:9], vcc
	s_cbranch_execz .LBB0_1078
	s_add_u32 s10, s30, 0x4200
	s_addc_u32 s11, s31, 0
	s_mov_b32 s34, 1
	s_mov_b64 s[14:15], 0
	v_mov_b32_e32 v1, 0
	s_branch .LBB0_1069

; __device__ __forceinline__ unsigned xb_ld(unsigned* p)              { return __hip_atomic_load(p, __ATOMIC_RELAXED, __HIP_MEMORY_SCOPE_AGENT); }
; __device__ __forceinline__ unsigned xb_add(unsigned* p, unsigned v) { return __hip_atomic_fetch_add(p, v, __ATOMIC_RELAXED, __HIP_MEMORY_SCOPE_AGENT); }
; #define XB_SPIN(cond, bar) do { unsigned _sp = 0; while (cond) { __builtin_amdgcn_s_sleep(1); \
;     if ((++_sp & 255u) == 0u) { if (xb_ld(&(bar)[XB_TMO])) break; if (_sp > XB_SPIN_CAP) { atomicAdd(&(bar)[XB_TMO], 1u); break; } } } } while (0)
; __device__ __forceinline__ void xcd_barrier(const XcdBarrier& b) {
;     ...
;         const unsigned old = xb_add(&bar[XB_XSUB(b.x)], 1u);
;         const unsigned gen = old / nloc;
;         if (old + 1u == (gen + 1u) * nloc) {
;             __builtin_amdgcn_fence(__ATOMIC_RELEASE, "agent");
;             asm volatile("s_waitcnt vmcnt(0)" ::: "memory");
;             const unsigned og = xb_add(&bar[XB_TOP], 1u);
;             const unsigned tg = og / nx;
;             if (og + 1u == (tg + 1u) * nx) xb_add(&bar[XB_TOPGEN], 1u);
;             else XB_SPIN(xb_ld(&bar[XB_TOPGEN]) == tg, bar);
;             __builtin_amdgcn_fence(__ATOMIC_ACQUIRE, "agent");
;             xb_add(&bar[XB_XGEN(b.x)], 1u);
;             asm volatile("s_waitcnt vmcnt(0)" ::: "memory");
;         } else {
;             XB_SPIN(xb_ld(&bar[XB_XGEN(b.x)]) == gen, bar);
;             __builtin_amdgcn_fence(__ATOMIC_ACQUIRE, "agent");
;             asm volatile("s_waitcnt vmcnt(0)" ::: "memory");
;         }
.LBB0_1368:
	v_readlane_b32 s4, v254, 29
	s_lshl_b32 s4, s4, 8
	v_readlane_b32 s6, v254, 27
	v_readlane_b32 s7, v254, 28
	s_add_u32 s4, s6, s4
	s_addc_u32 s5, s7, 0
	v_mov_b32_e32 v1, 0x1000
	v_mov_b32_e32 v3, 1
	global_atomic_add v3, v1, v3, s[4:5] offset:1024 sc0
	v_cvt_f32_u32_e32 v1, v2
	v_sub_u32_e32 v4, 0, v2
	v_rcp_iflag_f32_e32 v1, v1
	s_nop 0
	v_mul_f32_e32 v1, 0x4f7ffffe, v1
	v_cvt_u32_f32_e32 v1, v1
	v_mul_lo_u32 v4, v4, v1
	v_mul_hi_u32 v4, v1, v4
	v_add_u32_e32 v1, v1, v4
	s_waitcnt vmcnt(0)
	v_mul_hi_u32 v1, v3, v1
	v_mul_lo_u32 v4, v1, v2
	v_sub_u32_e32 v4, v3, v4
	v_add_u32_e32 v5, 1, v1
	v_cmp_ge_u32_e32 vcc, v4, v2
	v_add_u32_e32 v3, 1, v3
	s_nop 0
	v_cndmask_b32_e32 v1, v1, v5, vcc
	v_sub_u32_e32 v5, v4, v2
	v_cndmask_b32_e32 v4, v4, v5, vcc
	v_add_u32_e32 v5, 1, v1
	v_cmp_ge_u32_e32 vcc, v4, v2
	s_nop 1
	v_cndmask_b32_e32 v1, v1, v5, vcc
	v_mul_lo_u32 v4, v2, v1
	v_add_u32_e32 v2, v4, v2
	v_cmp_ne_u32_e32 vcc, v3, v2
	s_and_saveexec_b64 s[6:7], vcc
	s_xor_b64 s[6:7], exec, s[6:7]
	s_cbranch_execz .LBB0_1382
	s_waitcnt lgkmcnt(0)
	v_mov_b32_e32 v0, 0x2000
	s_add_u32 s12, s30, 0x7500
	s_addc_u32 s13, s31, 0
	v_mov_b32_e32 v0, 0
	global_load_dword v0, v0, s[12:13] sc1
	s_waitcnt vmcnt(0)
	v_cmp_eq_u32_e32 vcc, v0, v1
	s_and_saveexec_b64 s[8:9], vcc
	s_cbranch_execz .LBB0_1381
	s_add_u32 s10, s30, 0x4200
	s_addc_u32 s11, s31, 0
	s_mov_b32 s24, 1
	s_mov_b64 s[14:15], 0
	v_mov_b32_e32 v0, 0
	s_branch .LBB0_1372
